# grid barrier early L2 write-back moved from the 17th to the 25th arriver of each XCD (closer to the last arrival)
# speedup vs baseline: 1.0062x; 1.0062x over previous
.LBB0_265:
	v_readlane_b32 s4, v254, 37
	s_lshl_b32 s4, s4, 2
	s_add_u32 s25, s2, s4
	s_addc_u32 s24, s3, 0
	v_mov_b32_e32 v1, s25
	v_add_co_u32_e32 v4, vcc, 0x1000, v1
	v_mov_b32_e32 v1, s24
	s_nop 0
	v_addc_co_u32_e32 v5, vcc, 0, v1, vcc
	flat_atomic_add v3, v[4:5], v193 offset:1024 sc0
	v_cvt_f32_u32_e32 v1, v2
	v_sub_u32_e32 v4, 0, v2
	v_rcp_iflag_f32_e32 v1, v1
	s_nop 0
	v_mul_f32_e32 v1, 0x4f7ffffe, v1
	v_cvt_u32_f32_e32 v1, v1
	v_mul_lo_u32 v4, v4, v1
	v_mul_hi_u32 v4, v1, v4
	v_add_u32_e32 v1, v1, v4
	s_waitcnt vmcnt(0) lgkmcnt(0)
	v_and_b32_e32 v5, 31, v3
	v_cmp_eq_u32_e32 vcc, 24, v5
	s_nop 4
	s_cbranch_vccz .Lhalf_flush_11
	buffer_wbl2 sc1

.LBB0_353:
	v_readlane_b32 s4, v254, 37
	s_lshl_b32 s4, s4, 2
	s_add_u32 s27, s2, s4
	s_addc_u32 s26, s3, 0
	v_mov_b32_e32 v1, s27
	v_add_co_u32_e32 v4, vcc, 0x1000, v1
	v_mov_b32_e32 v1, s26
	s_nop 0
	v_addc_co_u32_e32 v5, vcc, 0, v1, vcc
	flat_atomic_add v3, v[4:5], v193 offset:1024 sc0
	v_cvt_f32_u32_e32 v1, v2
	v_sub_u32_e32 v4, 0, v2
	v_rcp_iflag_f32_e32 v1, v1
	s_nop 0
	v_mul_f32_e32 v1, 0x4f7ffffe, v1
	v_cvt_u32_f32_e32 v1, v1
	v_mul_lo_u32 v4, v4, v1
	v_mul_hi_u32 v4, v1, v4
	v_add_u32_e32 v1, v1, v4
	s_waitcnt vmcnt(0) lgkmcnt(0)
	v_and_b32_e32 v5, 31, v3
	v_cmp_eq_u32_e32 vcc, 24, v5
	s_nop 4
	s_cbranch_vccz .Lhalf_flush_10
	buffer_wbl2 sc1

.LBB0_583:
	v_readlane_b32 s6, v254, 37
	s_lshl_b32 s6, s6, 2
	s_add_u32 s30, s2, s6
	s_addc_u32 s29, s3, 0
	v_mov_b32_e32 v1, s30
	v_add_co_u32_e32 v4, vcc, 0x1000, v1
	v_mov_b32_e32 v1, s29
	s_nop 0
	v_addc_co_u32_e32 v5, vcc, 0, v1, vcc
	flat_atomic_add v3, v[4:5], v193 offset:1024 sc0
	v_cvt_f32_u32_e32 v1, v2
	v_sub_u32_e32 v4, 0, v2
	v_rcp_iflag_f32_e32 v1, v1
	s_nop 0
	v_mul_f32_e32 v1, 0x4f7ffffe, v1
	v_cvt_u32_f32_e32 v1, v1
	v_mul_lo_u32 v4, v4, v1
	v_mul_hi_u32 v4, v1, v4
	v_add_u32_e32 v1, v1, v4
	s_waitcnt vmcnt(0) lgkmcnt(0)
	v_and_b32_e32 v5, 31, v3
	v_cmp_eq_u32_e32 vcc, 24, v5
	s_nop 4
	s_cbranch_vccz .Lhalf_flush_7
	buffer_wbl2 sc1

.LBB0_689:
	v_readlane_b32 s4, v254, 37
	s_lshl_b32 s4, s4, 2
	s_add_u32 s9, s2, s4
	s_addc_u32 s8, s3, 0
	v_mov_b32_e32 v1, s9
	v_add_co_u32_e32 v4, vcc, 0x1000, v1
	v_mov_b32_e32 v1, s8
	s_nop 0
	v_addc_co_u32_e32 v5, vcc, 0, v1, vcc
	flat_atomic_add v3, v[4:5], v193 offset:1024 sc0
	v_cvt_f32_u32_e32 v1, v2
	v_sub_u32_e32 v4, 0, v2
	v_rcp_iflag_f32_e32 v1, v1
	s_nop 0
	v_mul_f32_e32 v1, 0x4f7ffffe, v1
	v_cvt_u32_f32_e32 v1, v1
	v_mul_lo_u32 v4, v4, v1
	v_mul_hi_u32 v4, v1, v4
	v_add_u32_e32 v1, v1, v4
	s_waitcnt vmcnt(0) lgkmcnt(0)
	v_and_b32_e32 v5, 31, v3
	v_cmp_eq_u32_e32 vcc, 24, v5
	s_nop 4
	s_cbranch_vccz .Lhalf_flush_6
	buffer_wbl2 sc1
